# EpiRes epilogue XR loads batched 8-deep plus per-CU start stagger in A8 and F2 phases
# speedup vs baseline: 1.0010x; 1.0010x over previous
.LBB0_1186:
	s_cmp_ge_i32 s36, s28
	s_cselect_b64 s[6:7], -1, 0
	s_and_b64 s[4:5], s[6:7], s[4:5]
	s_andn2_b64 vcc, exec, s[4:5]
	s_cbranch_vccnz .LBB0_1206
	s_waitcnt lgkmcnt(0)
	v_readlane_b32 s8, v254, 0
	s_nop 3
	s_cmp_lt_u32 s8, 16
	s_cbranch_scc1 .Lstg_a8_done
	s_mul_i32 s8, s8, 5
	s_and_b32 s8, s8, 15
	s_cmp_eq_u32 s8, 0
	s_cbranch_scc1 .Lstg_a8_done
.Lstg_a8_loop:
	s_sleep 20
	s_sub_u32 s8, s8, 1
	s_cmp_lg_u32 s8, 0
	s_cbranch_scc1 .Lstg_a8_loop
.Lstg_a8_done:
	v_readlane_b32 s8, v254, 3
	s_mov_b64 s[4:5], s[74:75]
	v_mov_b32_e32 v18, v0
	v_readlane_b32 s9, v254, 4
	s_load_dword s40, s[8:9], 0x0
	s_and_b64 s[8:9], s[64:65], exec
	s_movk_i32 s8, 0x80
	s_cselect_b32 s42, s8, 0x84
	v_readlane_b32 s41, v254, 0
	s_lshl_b32 s36, s42, 2
	s_waitcnt lgkmcnt(0)
	s_cmp_ge_i32 s41, s36
	v_readfirstlane_b32 s12, v18
	s_cbranch_scc1 .LBB0_1206
	v_lshlrev_b32_e32 v1, 4, v18
	v_add_u32_e32 v2, 0x2000, v1
	v_ashrrev_i32_e32 v4, 31, v2
	v_lshrrev_b32_e32 v4, 22, v4
	v_add_u32_e32 v4, v2, v4
	v_ashrrev_i32_e32 v12, 10, v4
	v_mul_i32_i24_e32 v4, 0x400, v12
	s_load_dwordx2 s[4:5], s[4:5], 0xd8
	v_sub_u32_e32 v2, v2, v4
	v_lshrrev_b32_e32 v4, 4, v2
	v_bitop3_b32 v2, v4, v2, 32 bitop3:0x6c
	v_ashrrev_i32_e32 v4, 31, v2
	v_lshrrev_b32_e32 v4, 26, v4
	v_readlane_b32 s20, v255, 20
	s_waitcnt lgkmcnt(0)
	s_add_u32 s43, s4, 0x2b100000
	v_add_u32_e32 v4, v2, v4
	v_lshlrev_b32_e32 v5, 3, v12
	s_mul_i32 s9, s20, 0xc10000
	s_addc_u32 s44, s5, 0
	v_ashrrev_i32_e32 v13, 6, v4
	v_and_b32_e32 v5, -16, v5
	s_mul_hi_u32 s8, s20, 0xc10000
	s_add_u32 s15, s4, s9
	v_add_u32_e32 v5, v13, v5
	s_addc_u32 s16, s5, s8
	v_and_b32_e32 v6, 3, v13
	s_mov_b32 s8, 0x1fffe0
	v_lshrrev_b32_e32 v7, 2, v5
	v_lshlrev_b32_e32 v8, 1, v5
	v_and_b32_e32 v4, 0xc0, v4
	v_and_or_b32 v6, v5, s8, v6
	v_and_b32_e32 v7, 4, v7
	v_and_b32_e32 v8, 24, v8
	v_sub_u32_e32 v2, v2, v4
	v_or3_b32 v6, v6, v7, v8
	v_lshlrev_b32_e32 v7, 5, v12
	v_ashrrev_i16_sdwa v2, v243, sext(v2) dst_sel:DWORD dst_unused:UNUSED_PAD src0_sel:DWORD src1_sel:BYTE_0
	v_and_b32_e32 v7, 32, v7
	v_bfe_i32 v14, v2, 0, 16
	v_add_lshl_u32 v2, v7, v14, 1
	v_lshl_add_u32 v148, v6, 11, v2
	v_lshl_add_u32 v150, v5, 11, v2
	v_bfe_i32 v2, v18, 27, 1
	v_lshrrev_b32_e32 v2, 22, v2
	v_add_u32_e32 v2, v1, v2
	v_and_b32_e32 v2, 0xfffffc00, v2
	v_sub_u32_e32 v1, v1, v2
	v_lshrrev_b32_e32 v2, 4, v1
	v_ashrrev_i32_e32 v4, 31, v18
	v_bitop3_b32 v1, v2, v1, 32 bitop3:0x6c
	v_lshrrev_b32_e32 v4, 26, v4
	v_ashrrev_i32_e32 v2, 31, v1
	v_add_u32_e32 v4, v18, v4
	v_lshrrev_b32_e32 v2, 26, v2
	v_ashrrev_i32_e32 v16, 6, v4
	v_add_u32_e32 v2, v1, v2
	v_lshlrev_b32_e32 v4, 3, v16
	s_add_u32 s45, s15, 0x1210000
	v_ashrrev_i32_e32 v15, 6, v2
	v_and_b32_e32 v4, -16, v4
	s_addc_u32 s46, s16, 0
	v_add_u32_e32 v4, v15, v4
	v_and_b32_e32 v5, 3, v15
	s_ashr_i32 s49, s41, 31
	v_and_or_b32 v5, v4, s8, v5
	s_lshr_b32 s8, s49, 29
	s_add_i32 s8, s41, s8
	s_ashr_i32 s13, s12, 6
	s_lshr_b32 s48, s42, 1
	s_ashr_i32 s9, s8, 3
	s_and_b32 s8, s8, -8
	s_ashr_i32 s14, s12, 8
	s_lshl_b32 s47, s13, 10
	s_sub_i32 s8, s41, s8
	s_or_b32 s50, s48, 1
	s_cmp_lt_i32 s8, 0
	s_cselect_b32 s10, s50, s48
	s_mul_i32 s8, s8, s10
	s_add_i32 s8, s8, s9
	s_ashr_i32 s9, s8, 31
	s_lshr_b32 s9, s9, 27
	s_add_i32 s9, s8, s9
	v_lshrrev_b32_e32 v6, 2, v4
	v_lshlrev_b32_e32 v7, 1, v4
	v_and_b32_e32 v2, 0xc0, v2
	s_ashr_i32 s10, s9, 5
	v_and_b32_e32 v6, 4, v6
	v_and_b32_e32 v7, 24, v7
	v_sub_u32_e32 v1, v1, v2
	s_andn2_b32 s9, s9, 31
	s_lshl_b32 s17, s10, 3
	v_or3_b32 v5, v5, v6, v7
	v_lshlrev_b32_e32 v6, 5, v16
	v_ashrrev_i16_sdwa v1, v243, sext(v1) dst_sel:DWORD dst_unused:UNUSED_PAD src0_sel:DWORD src1_sel:BYTE_0
	s_sub_i32 s11, s8, s9
	s_sub_i32 s8, s42, s17
	v_and_b32_e32 v6, 32, v6
	v_bfe_i32 v17, v1, 0, 16
	s_min_u32 s18, s8, 8
	v_add_lshl_u32 v1, v6, v17, 1
	v_cvt_f32_ubyte0_e32 v6, s18
	v_lshl_add_u32 v2, v5, 11, v1
	v_cvt_f32_i32_e32 v5, s11
	v_rcp_iflag_f32_e32 v7, v6
	v_lshl_add_u32 v152, v4, 11, v1
	s_ashr_i32 s8, s11, 30
	s_or_b32 s10, s8, 1
	v_mul_f32_e32 v1, v5, v7
	v_trunc_f32_e32 v1, v1
	v_fma_f32 v4, -v1, v6, v5
	v_cvt_i32_f32_e32 v1, v1
	v_cmp_ge_f32_e64 s[8:9], |v4|, v6
	s_and_b64 s[8:9], s[8:9], exec
	s_cselect_b32 s8, s10, 0
	v_readfirstlane_b32 s9, v1
	s_add_i32 s10, s9, s8
	s_mul_i32 s8, s10, s18
	s_sub_i32 s8, s11, s8
	s_sext_i32_i8 s8, s8
	s_add_i32 s17, s17, s8
	s_ashr_i32 s8, s17, 5
	s_add_i32 s11, s8, 1
	s_and_b64 s[8:9], s[64:65], exec
	s_cselect_b32 s8, s11, 0
	s_add_i32 s24, s8, s17
	s_ashr_i32 s25, s24, 31
	s_bfe_i64 s[18:19], s[10:11], 0x80000
	s_lshl_b64 s[8:9], s[24:25], 19
	s_lshl_b64 s[18:19], s[18:19], 19
	s_add_u32 s34, s45, s18
	s_addc_u32 s35, s46, s19
	s_add_i32 s51, s47, 0
	s_add_i32 m0, s51, 0x10000
	v_mov_b32_e32 v149, v3
	global_load_lds_dwordx4 v2, s[34:35]
	s_add_i32 m0, s51, 0x12000
	s_add_u32 s18, s34, 0x40000
	global_load_lds_dwordx4 v148, s[34:35]
	s_addc_u32 s19, s35, 0
	s_add_i32 m0, s51, 0x14000
	v_mov_b32_e32 v153, v3
	global_load_lds_dwordx4 v2, s[18:19]
	s_add_i32 m0, s51, 0x16000
	s_add_u32 s26, s43, s8
	s_addc_u32 s27, s44, s9
	s_add_i32 s52, s51, 0x2000
	global_load_lds_dwordx4 v148, s[18:19]
	s_mov_b32 m0, s51
	s_add_u32 s8, s26, 0x40000
	global_load_lds_dwordx4 v152, s[26:27]
	s_mov_b32 m0, s52
	s_addc_u32 s9, s27, 0
	s_add_i32 s53, s51, 0x4000
	global_load_lds_dwordx4 v150, s[26:27]
	s_mov_b32 m0, s53
	s_add_i32 s54, s51, 0x6000
	global_load_lds_dwordx4 v152, s[8:9]
	s_mov_b32 m0, s54
	v_mov_b32_e32 v151, v3
	global_load_lds_dwordx4 v150, s[8:9]
	s_cmp_eq_u32 s14, 1
	v_lshl_add_u64 v[10:11], s[34:35], 0, v[2:3]
	v_lshl_add_u64 v[8:9], s[34:35], 0, v[148:149]
	v_lshl_add_u64 v[4:5], s[26:27], 0, v[152:153]
	s_cselect_b64 s[8:9], -1, 0
	s_cmp_lg_u32 s14, 1
	v_lshl_add_u64 v[6:7], s[26:27], 0, v[150:151]
	s_cbranch_scc1 .LBB0_1190
	s_barrier

.LBB0_1758:
	s_cmp_ge_i32 s36, s28
	s_cselect_b64 s[8:9], -1, 0
	s_and_b64 s[4:5], s[8:9], s[4:5]
	s_andn2_b64 vcc, exec, s[4:5]
	s_cbranch_vccnz .LBB0_1782
	v_readlane_b32 s6, v254, 0
	s_nop 3
	s_cmp_lt_u32 s6, 16
	s_cbranch_scc1 .Lstg_f2_done
	s_mul_i32 s6, s6, 5
	s_and_b32 s6, s6, 15
	s_cmp_eq_u32 s6, 0
	s_cbranch_scc1 .Lstg_f2_done
.Lstg_f2_loop:
	s_sleep 20
	s_sub_u32 s6, s6, 1
	s_cmp_lg_u32 s6, 0
	s_cbranch_scc1 .Lstg_f2_loop
.Lstg_f2_done:
	v_readlane_b32 s6, v254, 3
	s_mov_b64 s[4:5], s[74:75]
	v_mov_b32_e32 v20, v0
	v_readlane_b32 s7, v254, 4
	s_load_dword s20, s[6:7], 0x0
	v_readlane_b32 s21, v254, 0
	s_waitcnt lgkmcnt(0)
	s_cmpk_gt_i32 s21, 0x20f
	v_readfirstlane_b32 s7, v20
	s_cbranch_scc1 .LBB0_1782
	v_lshlrev_b32_e32 v1, 4, v20
	v_add_u32_e32 v2, 0x2000, v1
	v_ashrrev_i32_e32 v4, 31, v2
	v_lshrrev_b32_e32 v4, 22, v4
	v_add_u32_e32 v4, v2, v4
	s_load_dwordx2 s[4:5], s[4:5], 0xd8
	v_ashrrev_i32_e32 v12, 10, v4
	v_mul_i32_i24_e32 v4, 0x400, v12
	v_sub_u32_e32 v2, v2, v4
	v_lshrrev_b32_e32 v4, 4, v2
	v_bitop3_b32 v2, v4, v2, 32 bitop3:0x6c
	s_waitcnt lgkmcnt(0)
	s_add_u32 s34, s4, 0x1ca00000
	v_readlane_b32 s17, v255, 20
	v_ashrrev_i32_e32 v4, 31, v2
	s_addc_u32 s35, s5, 0
	s_lshr_b32 s6, s17, 1
	v_lshrrev_b32_e32 v4, 26, v4
	s_mul_i32 s6, s6, 0x1080000
	v_add_u32_e32 v4, v2, v4
	v_lshlrev_b32_e32 v5, 3, v12
	s_add_u32 s6, s4, s6
	v_ashrrev_i32_e32 v13, 6, v4
	v_and_b32_e32 v5, -16, v5
	s_addc_u32 s10, s5, 0
	v_add_u32_e32 v5, v13, v5
	s_add_u32 s38, s6, 0x4500000
	v_and_b32_e32 v6, 3, v13
	s_mov_b32 s6, 0xffffe0
	v_lshrrev_b32_e32 v7, 2, v5
	v_lshlrev_b32_e32 v8, 1, v5
	v_and_b32_e32 v4, 0xc0, v4
	v_and_or_b32 v6, v5, s6, v6
	v_and_b32_e32 v7, 4, v7
	v_and_b32_e32 v8, 24, v8
	v_sub_u32_e32 v2, v2, v4
	v_or3_b32 v6, v6, v7, v8
	v_lshlrev_b32_e32 v7, 5, v12
	v_ashrrev_i16_sdwa v2, v243, sext(v2) dst_sel:DWORD dst_unused:UNUSED_PAD src0_sel:DWORD src1_sel:BYTE_0
	s_addc_u32 s39, s10, 0
	v_and_b32_e32 v14, 32, v7
	v_bfe_i32 v15, v2, 0, 16
	s_movk_i32 s10, 0xb00
	v_mul_u32_u24_e32 v6, 0xb00, v6
	v_add_u32_e32 v2, v14, v15
	v_mul_lo_u32 v4, v5, s10
	v_add_lshl_u32 v148, v6, v2, 1
	v_add_lshl_u32 v150, v2, v4, 1
	v_bfe_i32 v2, v20, 27, 1
	v_lshrrev_b32_e32 v2, 22, v2
	v_add_u32_e32 v2, v1, v2
	v_and_b32_e32 v2, 0xfffffc00, v2
	v_sub_u32_e32 v1, v1, v2
	v_lshrrev_b32_e32 v2, 4, v1
	v_ashrrev_i32_e32 v4, 31, v20
	v_bitop3_b32 v1, v2, v1, 32 bitop3:0x6c
	v_lshrrev_b32_e32 v4, 26, v4
	v_ashrrev_i32_e32 v2, 31, v1
	v_add_u32_e32 v4, v20, v4
	v_lshrrev_b32_e32 v2, 26, v2
	v_ashrrev_i32_e32 v17, 6, v4
	v_add_u32_e32 v2, v1, v2
	v_lshlrev_b32_e32 v4, 3, v17
	v_ashrrev_i32_e32 v16, 6, v2
	v_and_b32_e32 v4, -16, v4
	v_add_u32_e32 v4, v16, v4
	v_and_b32_e32 v5, 3, v16
	s_ashr_i32 s41, s21, 31
	v_and_or_b32 v5, v4, s6, v5
	s_lshr_b32 s6, s41, 29
	s_add_i32 s6, s21, s6
	s_ashr_i32 s14, s7, 6
	v_lshrrev_b32_e32 v6, 2, v4
	v_lshlrev_b32_e32 v7, 1, v4
	v_mul_lo_u32 v4, v4, s10
	s_ashr_i32 s10, s6, 3
	s_and_b32 s6, s6, -8
	s_ashr_i32 s15, s7, 8
	s_lshl_b32 s40, s14, 10
	s_sub_i32 s6, s21, s6
	s_cmp_lt_i32 s6, 0
	s_movk_i32 s11, 0x43
	s_cselect_b32 s11, s11, 0x42
	s_mul_i32 s6, s6, s11
	s_add_i32 s6, s6, s10
	s_ashr_i32 s10, s6, 31
	s_lshr_b32 s10, s10, 27
	s_add_i32 s10, s6, s10
	v_and_b32_e32 v2, 0xc0, v2
	s_ashr_i32 s11, s10, 5
	v_and_b32_e32 v6, 4, v6
	v_and_b32_e32 v7, 24, v7
	v_sub_u32_e32 v1, v1, v2
	s_andn2_b32 s10, s10, 31
	s_lshl_b32 s13, s11, 3
	v_or3_b32 v5, v5, v6, v7
	v_lshlrev_b32_e32 v6, 5, v17
	v_ashrrev_i16_sdwa v1, v243, sext(v1) dst_sel:DWORD dst_unused:UNUSED_PAD src0_sel:DWORD src1_sel:BYTE_0
	s_sub_i32 s12, s6, s10
	s_sub_i32 s6, 0x84, s13
	v_and_b32_e32 v18, 32, v6
	v_bfe_i32 v19, v1, 0, 16
	s_min_u32 s16, s6, 8
	v_mul_u32_u24_e32 v5, 0xb00, v5
	v_add_u32_e32 v1, v18, v19
	v_cvt_f32_ubyte0_e32 v6, s16
	v_add_lshl_u32 v2, v5, v1, 1
	v_cvt_f32_i32_e32 v5, s12
	v_rcp_iflag_f32_e32 v7, v6
	v_add_lshl_u32 v152, v1, v4, 1
	s_ashr_i32 s6, s12, 30
	s_or_b32 s6, s6, 1
	v_mul_f32_e32 v1, v5, v7
	v_trunc_f32_e32 v1, v1
	v_fma_f32 v4, -v1, v6, v5
	v_cvt_i32_f32_e32 v1, v1
	v_cmp_ge_f32_e64 s[10:11], |v4|, v6
	s_and_b64 s[10:11], s[10:11], exec
	s_cselect_b32 s6, s6, 0
	v_readfirstlane_b32 s10, v1
	s_add_i32 s6, s10, s6
	s_mul_i32 s10, s6, s16
	s_sub_i32 s10, s12, s10
	s_sext_i32_i8 s10, s10
	s_add_i32 s53, s13, s10
	s_bfe_i64 s[10:11], s[6:7], 0x80000
	s_mul_hi_i32 s11, s10, 0x160000
	s_mul_i32 s10, s10, 0x160000
	s_add_u32 s22, s38, s10
	s_addc_u32 s23, s39, s11
	s_add_i32 s42, s40, 0
	s_add_i32 m0, s42, 0x10000
	s_mul_i32 s13, s53, 0x160000
	global_load_lds_dwordx4 v2, s[22:23]
	s_add_i32 m0, s42, 0x12000
	s_add_u32 s10, s22, 0xb0000
	global_load_lds_dwordx4 v148, s[22:23]
	s_addc_u32 s11, s23, 0
	s_add_i32 m0, s42, 0x14000
	s_mul_hi_i32 s12, s53, 0x160000
	global_load_lds_dwordx4 v2, s[10:11]
	s_add_i32 m0, s42, 0x16000
	s_add_u32 s18, s34, s13
	s_addc_u32 s19, s35, s12
	s_add_i32 s43, s42, 0x2000
	global_load_lds_dwordx4 v148, s[10:11]
	s_mov_b32 m0, s42
	s_add_u32 s10, s18, 0xb0000
	global_load_lds_dwordx4 v152, s[18:19]
	s_mov_b32 m0, s43
	s_addc_u32 s11, s19, 0
	s_add_i32 s44, s42, 0x4000
	global_load_lds_dwordx4 v150, s[18:19]
	s_mov_b32 m0, s44
	s_add_i32 s45, s42, 0x6000
	global_load_lds_dwordx4 v152, s[10:11]
	s_mov_b32 m0, s45
	v_mov_b32_e32 v149, v3
	global_load_lds_dwordx4 v150, s[10:11]
	v_mov_b32_e32 v153, v3
	v_mov_b32_e32 v151, v3
	s_cmp_eq_u32 s15, 1
	v_lshl_add_u64 v[10:11], s[22:23], 0, v[2:3]
	v_lshl_add_u64 v[8:9], s[22:23], 0, v[148:149]
	v_lshl_add_u64 v[4:5], s[18:19], 0, v[152:153]
	s_cselect_b64 s[10:11], -1, 0
	s_cmp_lg_u32 s15, 1
	v_lshl_add_u64 v[6:7], s[18:19], 0, v[150:151]
	s_cbranch_scc1 .LBB0_1762
	s_barrier
